# relu2 w1: relaxed vmcnt(24) in first trip after epilogue (stores need not drain before next unit K-loop)
# baseline (speedup 1.0000x reference)
.LBB0_1220:
	v_and_b32_e32 v9, 15, v1
	v_and_b32_e32 v8, 48, v1
	v_lshlrev_b32_e32 v12, 2, v9
	s_sext_i32_i8 s58, s10
	s_and_b32 s45, s29, 3
	v_lshl_or_b32 v1, v9, 6, v8
	s_lshl_b32 s10, s28, 13
	v_and_b32_e32 v10, 32, v12
	s_lshl_b32 s29, s28, 6
	v_bitop3_b32 v13, v1, s10, v10 bitop3:0xde
	s_lshl_b32 s10, s45, 12
	s_add_u32 s16, s48, 0x8000
	s_addc_u32 s17, s49, 0
	v_bitop3_b32 v1, v1, s10, v10 bitop3:0xde
	s_add_i32 m0, s20, 0x18000
	v_lshl_add_u64 v[10:11], s[16:17], 0, v[114:115]
	v_mov_b32_e32 v137, v115
	s_waitcnt vmcnt(2)
	s_barrier
	global_load_lds_dwordx4 v[10:11], off
	s_add_i32 m0, s20, 0x1a000
	v_lshl_add_u64 v[10:11], s[16:17], 0, v[136:137]
	s_add_u32 s16, s46, 0x8000
	v_mov_b32_e32 v133, v115
	s_addc_u32 s17, s47, 0
	s_add_i32 s54, s20, 0x8000
	v_mov_b32_e32 v135, v115
	global_load_lds_dwordx4 v[10:11], off
	v_lshl_add_u64 v[10:11], s[16:17], 0, v[132:133]
	s_mov_b32 m0, s54
	s_add_i32 s55, s20, 0xa000
	global_load_lds_dwordx4 v[10:11], off
	v_lshl_add_u64 v[10:11], s[16:17], 0, v[134:135]
	s_add_u32 s16, s48, 0x9000
	s_mov_b32 m0, s55
	s_addc_u32 s17, s49, 0
	global_load_lds_dwordx4 v[10:11], off
	s_add_i32 m0, s20, 0x1c000
	v_lshl_add_u64 v[10:11], s[16:17], 0, v[114:115]
	global_load_lds_dwordx4 v[10:11], off
	v_lshl_add_u64 v[10:11], s[16:17], 0, v[136:137]
	s_add_i32 m0, s20, 0x1e000
	s_cmpk_lt_u32 s11, 0x100
	global_load_lds_dwordx4 v[10:11], off
	s_cselect_b64 s[10:11], -1, 0
	s_ashr_i32 s16, s29, 31
	v_or_b32_e32 v10, s29, v9
	v_mov_b32_e32 v11, s16
	v_lshlrev_b64 v[10:11], 7, v[10:11]
	v_lshl_add_u64 v[10:11], s[26:27], 0, v[10:11]
	v_mov_b32_e32 v9, v115
	v_lshl_add_u64 v[8:9], v[10:11], 0, v[8:9]
	s_mov_b64 s[16:17], 0x28100000
	v_lshl_add_u64 v[138:139], v[8:9], 0, s[16:17]
	v_lshlrev_b32_e32 v8, 10, v2
	v_and_b32_e32 v8, 0xfffff800, v8
	v_lshl_add_u32 v3, v3, 7, v8
	v_and_b32_e32 v2, 1, v2
	v_lshl_or_b32 v2, v2, 6, v3
	v_lshl_add_u32 v140, v4, 1, v2
	v_lshlrev_b32_e32 v2, 10, v5
	s_lshl_b32 s16, s28, 8
	v_and_b32_e32 v2, 0xfffff800, v2
	s_waitcnt vmcnt(6)
	s_add_i32 s16, s16, 0
	v_lshl_add_u32 v2, v6, 7, v2
	v_and_b32_e32 v3, 1, v5
	s_add_i32 s16, s16, 0x20400
	v_lshl_or_b32 v2, v3, 6, v2
	v_add_u32_e32 v146, s16, v12
	v_mov_b32_e32 v141, v115
	v_lshl_add_u32 v142, v7, 1, v2
	v_mov_b32_e32 v143, v115
	s_mov_b32 s59, 0
	v_add_u32_e32 v147, 0, v13
	s_mov_b32 s56, 0
	s_barrier
	s_waitcnt vmcnt(0)
	s_mov_b32 s32, 0
	s_branch .LBB0_1223
.LBB0_1221:
	s_mov_b64 s[38:39], 0
	s_mov_b32 s32, 1

.LBB0_1230:
	s_add_u32 s16, s46, 0x4000
	s_addc_u32 s17, s47, 0
	s_cmp_eq_u32 s64, 28
	s_cselect_b32 s52, s60, s16
	s_cselect_b32 s53, s29, s17
	s_cselect_b32 s51, s27, s63
	s_cselect_b32 s50, s61, s62
	s_add_u32 s48, s52, 0x8000
	s_addc_u32 s49, s53, 0
	s_add_i32 s16, 0, 0x10000
	v_add_u32_e32 v144, s16, v1
	s_add_i32 s65, 0, 0x14000
	ds_read_b128 v[148:151], v144
	ds_read_b128 v[152:155], v144 offset:1024
	ds_read_b128 v[158:161], v144 offset:2048
	ds_read_b128 v[166:169], v144 offset:3072
	v_add_u32_e32 v144, s65, v1
	ds_read_b128 v[170:173], v144
	ds_read_b128 v[174:177], v144 offset:1024
	ds_read_b128 v[178:181], v144 offset:2048
	ds_read_b128 v[194:197], v144 offset:3072
	v_lshl_add_u64 v[144:145], s[46:47], 0, v[140:141]
	s_add_i32 m0, s20, 0xc000
	ds_read_b128 v[198:201], v147
	ds_read_b128 v[202:205], v147 offset:1024
	ds_read_b128 v[206:209], v147 offset:2048
	ds_read_b128 v[210:213], v147 offset:3072
	ds_read_b128 v[214:217], v147 offset:4096
	ds_read_b128 v[218:221], v147 offset:5120
	ds_read_b128 v[222:225], v147 offset:6144
	ds_read_b128 v[226:229], v147 offset:7168
	global_load_lds_dwordx4 v[144:145], off
	v_lshl_add_u64 v[144:145], s[46:47], 0, v[142:143]
	s_add_i32 m0, s20, 0xe000
	s_nop 0
	global_load_lds_dwordx4 v[144:145], off
	s_cmp_lg_u32 s32, 0
	s_cbranch_scc1 .Lrx_relu2_a
	s_waitcnt vmcnt(8)
.Lrx_relu2_a:
	s_waitcnt vmcnt(24)
	s_waitcnt lgkmcnt(0)
	s_barrier
	s_setprio 1
	s_waitcnt lgkmcnt(0)
	v_mfma_f32_16x16x32_bf16 v[128:131], v[148:151], v[198:201], v[128:131]
	v_mfma_f32_16x16x32_bf16 v[124:127], v[158:161], v[198:201], v[124:127]
	v_mfma_f32_16x16x32_bf16 v[110:113], v[148:151], v[206:209], v[110:113]
	v_mfma_f32_16x16x32_bf16 v[106:109], v[158:161], v[206:209], v[106:109]
	v_mfma_f32_16x16x32_bf16 v[94:97], v[148:151], v[214:217], v[94:97]
	v_mfma_f32_16x16x32_bf16 v[90:93], v[158:161], v[214:217], v[90:93]
	v_mfma_f32_16x16x32_bf16 v[78:81], v[148:151], v[222:225], v[78:81]
	v_mfma_f32_16x16x32_bf16 v[74:77], v[158:161], v[222:225], v[74:77]
	v_mfma_f32_16x16x32_bf16 v[128:131], v[152:155], v[202:205], v[128:131]
	v_mfma_f32_16x16x32_bf16 v[124:127], v[166:169], v[202:205], v[124:127]
	v_mfma_f32_16x16x32_bf16 v[110:113], v[152:155], v[210:213], v[110:113]
	v_mfma_f32_16x16x32_bf16 v[106:109], v[166:169], v[210:213], v[106:109]
	v_mfma_f32_16x16x32_bf16 v[94:97], v[152:155], v[218:221], v[94:97]
	v_mfma_f32_16x16x32_bf16 v[90:93], v[166:169], v[218:221], v[90:93]
	v_mfma_f32_16x16x32_bf16 v[78:81], v[152:155], v[226:229], v[78:81]
	v_mfma_f32_16x16x32_bf16 v[74:77], v[166:169], v[226:229], v[74:77]
	s_setprio 0
	s_setprio 1
	v_mfma_f32_16x16x32_bf16 v[120:123], v[170:173], v[198:201], v[120:123]
	v_mfma_f32_16x16x32_bf16 v[116:119], v[178:181], v[198:201], v[116:119]
	v_mfma_f32_16x16x32_bf16 v[102:105], v[170:173], v[206:209], v[102:105]
	v_mfma_f32_16x16x32_bf16 v[98:101], v[178:181], v[206:209], v[98:101]
	v_mfma_f32_16x16x32_bf16 v[86:89], v[170:173], v[214:217], v[86:89]
	v_mfma_f32_16x16x32_bf16 v[82:85], v[178:181], v[214:217], v[82:85]
	v_mfma_f32_16x16x32_bf16 v[70:73], v[170:173], v[222:225], v[70:73]
	v_mfma_f32_16x16x32_bf16 v[66:69], v[178:181], v[222:225], v[66:69]
	v_mfma_f32_16x16x32_bf16 v[120:123], v[174:177], v[202:205], v[120:123]
	v_mfma_f32_16x16x32_bf16 v[116:119], v[194:197], v[202:205], v[116:119]
	v_mfma_f32_16x16x32_bf16 v[102:105], v[174:177], v[210:213], v[102:105]
	v_mfma_f32_16x16x32_bf16 v[98:101], v[194:197], v[210:213], v[98:101]
	v_mfma_f32_16x16x32_bf16 v[86:89], v[174:177], v[218:221], v[86:89]
	v_mfma_f32_16x16x32_bf16 v[82:85], v[194:197], v[218:221], v[82:85]
	v_mfma_f32_16x16x32_bf16 v[70:73], v[174:177], v[226:229], v[70:73]
	v_mfma_f32_16x16x32_bf16 v[66:69], v[194:197], v[226:229], v[66:69]
	s_setprio 0
	s_barrier
	s_add_i32 s16, s16, s7
	v_lshl_add_u64 v[144:145], s[50:51], 0, v[114:115]
	s_mov_b32 m0, s16
	ds_read_b128 v[198:201], v147 offset:16384
	ds_read_b128 v[202:205], v147 offset:17408
	ds_read_b128 v[206:209], v147 offset:18432
	ds_read_b128 v[210:213], v147 offset:19456
	ds_read_b128 v[214:217], v147 offset:20480
	ds_read_b128 v[218:221], v147 offset:21504
	ds_read_b128 v[222:225], v147 offset:22528
	ds_read_b128 v[226:229], v147 offset:23552
	global_load_lds_dwordx4 v[144:145], off
	s_add_i32 m0, s16, 0x2000
	s_add_u32 s16, s50, 0x1000
	v_lshl_add_u64 v[144:145], s[50:51], 0, v[136:137]
	s_addc_u32 s17, s51, 0
	s_add_i32 s65, s65, s7
	global_load_lds_dwordx4 v[144:145], off
	v_lshl_add_u64 v[144:145], s[16:17], 0, v[114:115]
	s_mov_b32 m0, s65
	s_nop 0
	global_load_lds_dwordx4 v[144:145], off
	v_lshl_add_u64 v[144:145], s[16:17], 0, v[136:137]
	s_add_i32 m0, s65, 0x2000
	s_nop 0
	global_load_lds_dwordx4 v[144:145], off
	v_lshl_add_u64 v[144:145], s[52:53], 0, v[132:133]
	s_mov_b32 m0, s20
	s_nop 0
	global_load_lds_dwordx4 v[144:145], off
	v_lshl_add_u64 v[144:145], s[52:53], 0, v[134:135]
	s_mov_b32 m0, s21
	s_nop 0
	global_load_lds_dwordx4 v[144:145], off
	s_cmp_lg_u32 s32, 0
	s_cbranch_scc1 .Lrx_relu2_b
	s_waitcnt vmcnt(8)
.Lrx_relu2_b:
	s_waitcnt vmcnt(24)
	s_mov_b32 s32, 0
	s_waitcnt lgkmcnt(0)
	s_barrier
	s_setprio 1
	s_waitcnt lgkmcnt(0)
	v_mfma_f32_16x16x32_bf16 v[62:65], v[148:151], v[198:201], v[62:65]
	v_mfma_f32_16x16x32_bf16 v[58:61], v[158:161], v[198:201], v[58:61]
	v_mfma_f32_16x16x32_bf16 v[46:49], v[148:151], v[206:209], v[46:49]
	v_mfma_f32_16x16x32_bf16 v[42:45], v[158:161], v[206:209], v[42:45]
	v_mfma_f32_16x16x32_bf16 v[30:33], v[148:151], v[214:217], v[30:33]
	v_mfma_f32_16x16x32_bf16 v[26:29], v[158:161], v[214:217], v[26:29]
	v_mfma_f32_16x16x32_bf16 v[14:17], v[148:151], v[222:225], v[14:17]
	v_mfma_f32_16x16x32_bf16 v[10:13], v[158:161], v[222:225], v[10:13]
	v_mfma_f32_16x16x32_bf16 v[62:65], v[152:155], v[202:205], v[62:65]
	v_mfma_f32_16x16x32_bf16 v[58:61], v[166:169], v[202:205], v[58:61]
	v_mfma_f32_16x16x32_bf16 v[46:49], v[152:155], v[210:213], v[46:49]
	v_mfma_f32_16x16x32_bf16 v[42:45], v[166:169], v[210:213], v[42:45]
	v_mfma_f32_16x16x32_bf16 v[30:33], v[152:155], v[218:221], v[30:33]
	v_mfma_f32_16x16x32_bf16 v[26:29], v[166:169], v[218:221], v[26:29]
	v_mfma_f32_16x16x32_bf16 v[14:17], v[152:155], v[226:229], v[14:17]
	v_mfma_f32_16x16x32_bf16 v[10:13], v[166:169], v[226:229], v[10:13]
	s_setprio 0
	s_setprio 1
	v_mfma_f32_16x16x32_bf16 v[54:57], v[170:173], v[198:201], v[54:57]
	v_mfma_f32_16x16x32_bf16 v[50:53], v[178:181], v[198:201], v[50:53]
	v_mfma_f32_16x16x32_bf16 v[38:41], v[170:173], v[206:209], v[38:41]
	v_mfma_f32_16x16x32_bf16 v[34:37], v[178:181], v[206:209], v[34:37]
	v_mfma_f32_16x16x32_bf16 v[22:25], v[170:173], v[214:217], v[22:25]
	v_mfma_f32_16x16x32_bf16 v[18:21], v[178:181], v[214:217], v[18:21]
	v_mfma_f32_16x16x32_bf16 v[6:9], v[170:173], v[222:225], v[6:9]
	v_mfma_f32_16x16x32_bf16 v[2:5], v[178:181], v[222:225], v[2:5]
	v_mfma_f32_16x16x32_bf16 v[54:57], v[174:177], v[202:205], v[54:57]
	v_mfma_f32_16x16x32_bf16 v[50:53], v[194:197], v[202:205], v[50:53]
	v_mfma_f32_16x16x32_bf16 v[38:41], v[174:177], v[210:213], v[38:41]
	v_mfma_f32_16x16x32_bf16 v[34:37], v[194:197], v[210:213], v[34:37]
	v_mfma_f32_16x16x32_bf16 v[22:25], v[174:177], v[218:221], v[22:25]
	v_mfma_f32_16x16x32_bf16 v[18:21], v[194:197], v[218:221], v[18:21]
	v_mfma_f32_16x16x32_bf16 v[6:9], v[174:177], v[226:229], v[6:9]
	v_mfma_f32_16x16x32_bf16 v[2:5], v[194:197], v[226:229], v[2:5]
	s_setprio 0
	s_barrier
	s_add_i32 s65, 0, 0x18000
	v_add_u32_e32 v144, s65, v1
	s_add_i32 s66, 0, 0x1c000
	ds_read_b128 v[148:151], v144
	ds_read_b128 v[152:155], v144 offset:1024
	ds_read_b128 v[158:161], v144 offset:2048
	ds_read_b128 v[166:169], v144 offset:3072
	v_add_u32_e32 v144, s66, v1
	ds_read_b128 v[170:173], v144
	ds_read_b128 v[174:177], v144 offset:1024
	ds_read_b128 v[178:181], v144 offset:2048
	ds_read_b128 v[194:197], v144 offset:3072
	s_add_u32 s16, s52, 0x4000
	s_addc_u32 s17, s53, 0
	s_mov_b32 m0, s24
	v_lshl_add_u64 v[144:145], s[16:17], 0, v[132:133]
	ds_read_b128 v[198:201], v147 offset:32768
	ds_read_b128 v[202:205], v147 offset:33792
	ds_read_b128 v[206:209], v147 offset:34816
	ds_read_b128 v[210:213], v147 offset:35840
	ds_read_b128 v[214:217], v147 offset:36864
	ds_read_b128 v[218:221], v147 offset:37888
	ds_read_b128 v[222:225], v147 offset:38912
	ds_read_b128 v[226:229], v147 offset:39936
	global_load_lds_dwordx4 v[144:145], off
	v_lshl_add_u64 v[144:145], s[16:17], 0, v[134:135]
	s_mov_b32 m0, s37
	s_nop 0
	global_load_lds_dwordx4 v[144:145], off
	s_waitcnt vmcnt(8)
	s_waitcnt lgkmcnt(0)
	s_barrier
	s_setprio 1
	s_waitcnt lgkmcnt(0)
	v_mfma_f32_16x16x32_bf16 v[128:131], v[148:151], v[198:201], v[128:131]
	v_mfma_f32_16x16x32_bf16 v[124:127], v[158:161], v[198:201], v[124:127]
	v_mfma_f32_16x16x32_bf16 v[110:113], v[148:151], v[206:209], v[110:113]
	v_mfma_f32_16x16x32_bf16 v[106:109], v[158:161], v[206:209], v[106:109]
	v_mfma_f32_16x16x32_bf16 v[94:97], v[148:151], v[214:217], v[94:97]
	v_mfma_f32_16x16x32_bf16 v[90:93], v[158:161], v[214:217], v[90:93]
	v_mfma_f32_16x16x32_bf16 v[78:81], v[148:151], v[222:225], v[78:81]
	v_mfma_f32_16x16x32_bf16 v[74:77], v[158:161], v[222:225], v[74:77]
	v_mfma_f32_16x16x32_bf16 v[128:131], v[152:155], v[202:205], v[128:131]
	v_mfma_f32_16x16x32_bf16 v[124:127], v[166:169], v[202:205], v[124:127]
	v_mfma_f32_16x16x32_bf16 v[110:113], v[152:155], v[210:213], v[110:113]
	v_mfma_f32_16x16x32_bf16 v[106:109], v[166:169], v[210:213], v[106:109]
	v_mfma_f32_16x16x32_bf16 v[94:97], v[152:155], v[218:221], v[94:97]
	v_mfma_f32_16x16x32_bf16 v[90:93], v[166:169], v[218:221], v[90:93]
	v_mfma_f32_16x16x32_bf16 v[78:81], v[152:155], v[226:229], v[78:81]
	v_mfma_f32_16x16x32_bf16 v[74:77], v[166:169], v[226:229], v[74:77]
	s_setprio 0
	s_setprio 1
	v_mfma_f32_16x16x32_bf16 v[120:123], v[170:173], v[198:201], v[120:123]
	v_mfma_f32_16x16x32_bf16 v[116:119], v[178:181], v[198:201], v[116:119]
	v_mfma_f32_16x16x32_bf16 v[102:105], v[170:173], v[206:209], v[102:105]
	v_mfma_f32_16x16x32_bf16 v[98:101], v[178:181], v[206:209], v[98:101]
	v_mfma_f32_16x16x32_bf16 v[86:89], v[170:173], v[214:217], v[86:89]
	v_mfma_f32_16x16x32_bf16 v[82:85], v[178:181], v[214:217], v[82:85]
	v_mfma_f32_16x16x32_bf16 v[70:73], v[170:173], v[222:225], v[70:73]
	v_mfma_f32_16x16x32_bf16 v[66:69], v[178:181], v[222:225], v[66:69]
	v_mfma_f32_16x16x32_bf16 v[120:123], v[174:177], v[202:205], v[120:123]
	v_mfma_f32_16x16x32_bf16 v[116:119], v[194:197], v[202:205], v[116:119]
	v_mfma_f32_16x16x32_bf16 v[102:105], v[174:177], v[210:213], v[102:105]
	v_mfma_f32_16x16x32_bf16 v[98:101], v[194:197], v[210:213], v[98:101]
	v_mfma_f32_16x16x32_bf16 v[86:89], v[174:177], v[218:221], v[86:89]
	v_mfma_f32_16x16x32_bf16 v[82:85], v[194:197], v[218:221], v[82:85]
	v_mfma_f32_16x16x32_bf16 v[70:73], v[174:177], v[226:229], v[70:73]
	v_mfma_f32_16x16x32_bf16 v[66:69], v[194:197], v[226:229], v[66:69]
	s_setprio 0
	s_barrier
	s_add_u32 s16, s50, 0x8000
	s_addc_u32 s17, s51, 0
	s_add_i32 s52, s65, s7
	v_lshl_add_u64 v[144:145], s[16:17], 0, v[114:115]
	s_mov_b32 m0, s52
	ds_read_b128 v[198:201], v147 offset:49152
	ds_read_b128 v[202:205], v147 offset:50176
	ds_read_b128 v[206:209], v147 offset:51200
	ds_read_b128 v[210:213], v147 offset:52224
	ds_read_b128 v[214:217], v147 offset:53248
	ds_read_b128 v[218:221], v147 offset:54272
	ds_read_b128 v[222:225], v147 offset:55296
	ds_read_b128 v[226:229], v147 offset:56320
	global_load_lds_dwordx4 v[144:145], off
	s_add_i32 m0, s52, 0x2000
	v_lshl_add_u64 v[144:145], s[16:17], 0, v[136:137]
	s_add_u32 s16, s50, 0x9000
	s_addc_u32 s17, s51, 0
	s_add_i32 s50, s66, s7
	global_load_lds_dwordx4 v[144:145], off
	v_lshl_add_u64 v[144:145], s[16:17], 0, v[114:115]
	s_mov_b32 m0, s50
	s_nop 0
	global_load_lds_dwordx4 v[144:145], off
	v_lshl_add_u64 v[144:145], s[16:17], 0, v[136:137]
	s_add_i32 m0, s50, 0x2000
	s_nop 0
	global_load_lds_dwordx4 v[144:145], off
	v_lshl_add_u64 v[144:145], s[48:49], 0, v[132:133]
	s_mov_b32 m0, s54
	s_nop 0
	global_load_lds_dwordx4 v[144:145], off
	v_lshl_add_u64 v[144:145], s[48:49], 0, v[134:135]
	s_mov_b32 m0, s55
	s_nop 0
	global_load_lds_dwordx4 v[144:145], off
	s_waitcnt vmcnt(8)
	s_waitcnt lgkmcnt(0)
	s_barrier
	s_setprio 1
	s_waitcnt lgkmcnt(0)
	v_mfma_f32_16x16x32_bf16 v[62:65], v[148:151], v[198:201], v[62:65]
	v_mfma_f32_16x16x32_bf16 v[58:61], v[158:161], v[198:201], v[58:61]
	v_mfma_f32_16x16x32_bf16 v[46:49], v[148:151], v[206:209], v[46:49]
	v_mfma_f32_16x16x32_bf16 v[42:45], v[158:161], v[206:209], v[42:45]
	v_mfma_f32_16x16x32_bf16 v[30:33], v[148:151], v[214:217], v[30:33]
	v_mfma_f32_16x16x32_bf16 v[26:29], v[158:161], v[214:217], v[26:29]
	v_mfma_f32_16x16x32_bf16 v[14:17], v[148:151], v[222:225], v[14:17]
	v_mfma_f32_16x16x32_bf16 v[10:13], v[158:161], v[222:225], v[10:13]
	v_mfma_f32_16x16x32_bf16 v[62:65], v[152:155], v[202:205], v[62:65]
	v_mfma_f32_16x16x32_bf16 v[58:61], v[166:169], v[202:205], v[58:61]
	v_mfma_f32_16x16x32_bf16 v[46:49], v[152:155], v[210:213], v[46:49]
	v_mfma_f32_16x16x32_bf16 v[42:45], v[166:169], v[210:213], v[42:45]
	v_mfma_f32_16x16x32_bf16 v[30:33], v[152:155], v[218:221], v[30:33]
	v_mfma_f32_16x16x32_bf16 v[26:29], v[166:169], v[218:221], v[26:29]
	v_mfma_f32_16x16x32_bf16 v[14:17], v[152:155], v[226:229], v[14:17]
	v_mfma_f32_16x16x32_bf16 v[10:13], v[166:169], v[226:229], v[10:13]
	s_setprio 0
	s_setprio 1
	v_mfma_f32_16x16x32_bf16 v[54:57], v[170:173], v[198:201], v[54:57]
	v_mfma_f32_16x16x32_bf16 v[50:53], v[178:181], v[198:201], v[50:53]
	v_mfma_f32_16x16x32_bf16 v[38:41], v[170:173], v[206:209], v[38:41]
	v_mfma_f32_16x16x32_bf16 v[34:37], v[178:181], v[206:209], v[34:37]
	v_mfma_f32_16x16x32_bf16 v[22:25], v[170:173], v[214:217], v[22:25]
	v_mfma_f32_16x16x32_bf16 v[18:21], v[178:181], v[214:217], v[18:21]
	v_mfma_f32_16x16x32_bf16 v[6:9], v[170:173], v[222:225], v[6:9]
	v_mfma_f32_16x16x32_bf16 v[2:5], v[178:181], v[222:225], v[2:5]
	v_mfma_f32_16x16x32_bf16 v[54:57], v[174:177], v[202:205], v[54:57]
	v_mfma_f32_16x16x32_bf16 v[50:53], v[194:197], v[202:205], v[50:53]
	v_mfma_f32_16x16x32_bf16 v[38:41], v[174:177], v[210:213], v[38:41]
	v_mfma_f32_16x16x32_bf16 v[34:37], v[194:197], v[210:213], v[34:37]
	v_mfma_f32_16x16x32_bf16 v[22:25], v[174:177], v[218:221], v[22:25]
	v_mfma_f32_16x16x32_bf16 v[18:21], v[194:197], v[218:221], v[18:21]
	v_mfma_f32_16x16x32_bf16 v[6:9], v[174:177], v[226:229], v[6:9]
	v_mfma_f32_16x16x32_bf16 v[2:5], v[194:197], v[226:229], v[2:5]
	s_setprio 0
	s_barrier
	s_add_i32 s64, s64, 2
	s_add_u32 s46, s46, 0x10000
	s_addc_u32 s47, s47, 0
	s_add_u32 s62, s62, 0x10000
	s_addc_u32 s63, s63, 0
	s_cmp_gt_u32 s64, 29
	s_cbranch_scc0 .LBB0_1230
	s_and_b64 vcc, exec, s[10:11]
	s_cbranch_vccz .LBB0_1233
	s_barrier
